# N1 router-weight LDS staging: 16 dependent load->convert->ds_write iterations unrolled so all 16 loads are in flight (counted vmcnt), packed cvt + d16_hi writes
# baseline (speedup 1.0000x reference)
; #define LAS __attribute__((address_space(3)))
; DI unsigned pk2(float lo, float hi) { f32x2 v = {lo, hi}; bf16x2v r = __builtin_convertvector(v, bf16x2v); return __builtin_bit_cast(unsigned, r); }
; DI void phase_n1(Frame& F, int l) {
;     ...
;     for (int idx = F.tid; idx < D * 8; idx += 512) { const int k = idx >> 3, c = idx & 7; const f32x4 v = *(const f32x4*)(wr_ + k * 32 + 4 * c);
; #pragma unroll
;         for (int q = 0; q < 4; ++q) *(LAS bf16_t*)(WTl + (4 * c + q) * RP + k * 2) = (bf16_t)(pk2(v[q], 0.f) & 0xffffu); }
;     __syncthreads();
.LBB0_1024:
	s_or_b64 exec, exec, s[2:3]
	s_mov_b32 s0, -1
	s_waitcnt lgkmcnt(0)
	s_barrier
	s_mov_b64 s[20:21], s[70:71]
	v_mbcnt_lo_u32_b32 v0, s0, 0
	v_mbcnt_hi_u32_b32 v2, s0, v0
	v_readlane_b32 s0, v253, 29
	s_mov_b32 s30, s0
	v_lshl_add_u32 v3, s97, 6, v2
	s_movk_i32 s0, 0x2000
	v_cmp_gt_i32_e32 vcc, s0, v3
	v_readlane_b32 s1, v253, 30
	s_and_saveexec_b64 s[2:3], vcc
	s_cbranch_execz .LBB0_1027
	s_load_dwordx2 s[0:1], s[20:21], 0xb0
	v_readlane_b32 s4, v255, 14
	v_readlane_b32 s5, v255, 15
	s_lshl_b64 s[4:5], s[4:5], 17
	v_lshlrev_b32_e32 v0, 2, v2
	s_waitcnt lgkmcnt(0)
	s_add_u32 s4, s0, s4
	s_addc_u32 s5, s1, s5
	v_lshl_add_u32 v4, s97, 8, v0
	v_ashrrev_i32_e32 v10, 3, v3
	v_and_b32_e32 v11, 28, v4
	v_lshlrev_b32_e32 v6, 7, v10
	v_lshl_add_u32 v6, v11, 2, v6
	v_lshlrev_b32_e32 v10, 1, v10
	v_mul_u32_u24_e32 v11, 0x810, v11
	v_add3_u32 v0, 0, v10, v11
	global_load_dwordx4 v[16:19], v6, s[4:5]
	s_add_u32 s4, s4, 0x2000
	s_addc_u32 s5, s5, 0
	global_load_dwordx4 v[20:23], v6, s[4:5]
	s_add_u32 s4, s4, 0x2000
	s_addc_u32 s5, s5, 0
	global_load_dwordx4 v[24:27], v6, s[4:5]
	s_add_u32 s4, s4, 0x2000
	s_addc_u32 s5, s5, 0
	global_load_dwordx4 v[28:31], v6, s[4:5]
	s_add_u32 s4, s4, 0x2000
	s_addc_u32 s5, s5, 0
	global_load_dwordx4 v[32:35], v6, s[4:5]
	s_add_u32 s4, s4, 0x2000
	s_addc_u32 s5, s5, 0
	global_load_dwordx4 v[36:39], v6, s[4:5]
	s_add_u32 s4, s4, 0x2000
	s_addc_u32 s5, s5, 0
	global_load_dwordx4 v[40:43], v6, s[4:5]
	s_add_u32 s4, s4, 0x2000
	s_addc_u32 s5, s5, 0
	global_load_dwordx4 v[44:47], v6, s[4:5]
	s_add_u32 s4, s4, 0x2000
	s_addc_u32 s5, s5, 0
	global_load_dwordx4 v[48:51], v6, s[4:5]
	s_add_u32 s4, s4, 0x2000
	s_addc_u32 s5, s5, 0
	global_load_dwordx4 v[52:55], v6, s[4:5]
	s_add_u32 s4, s4, 0x2000
	s_addc_u32 s5, s5, 0
	global_load_dwordx4 v[56:59], v6, s[4:5]
	s_add_u32 s4, s4, 0x2000
	s_addc_u32 s5, s5, 0
	global_load_dwordx4 v[60:63], v6, s[4:5]
	s_add_u32 s4, s4, 0x2000
	s_addc_u32 s5, s5, 0
	global_load_dwordx4 v[64:67], v6, s[4:5]
	s_add_u32 s4, s4, 0x2000
	s_addc_u32 s5, s5, 0
	global_load_dwordx4 v[68:71], v6, s[4:5]
	s_add_u32 s4, s4, 0x2000
	s_addc_u32 s5, s5, 0
	global_load_dwordx4 v[72:75], v6, s[4:5]
	s_add_u32 s4, s4, 0x2000
	s_addc_u32 s5, s5, 0
	global_load_dwordx4 v[76:79], v6, s[4:5]
	s_waitcnt vmcnt(15)
	v_cvt_pk_bf16_f32 v16, v16, v17
	v_cvt_pk_bf16_f32 v18, v18, v19
	ds_write_b16 v0, v16
	ds_write_b16_d16_hi v0, v16 offset:2064
	ds_write_b16 v0, v18 offset:4128
	ds_write_b16_d16_hi v0, v18 offset:6192
	s_waitcnt vmcnt(14)
	v_cvt_pk_bf16_f32 v20, v20, v21
	v_cvt_pk_bf16_f32 v22, v22, v23
	ds_write_b16 v0, v20 offset:128
	ds_write_b16_d16_hi v0, v20 offset:2192
	ds_write_b16 v0, v22 offset:4256
	ds_write_b16_d16_hi v0, v22 offset:6320
	s_waitcnt vmcnt(13)
	v_cvt_pk_bf16_f32 v24, v24, v25
	v_cvt_pk_bf16_f32 v26, v26, v27
	ds_write_b16 v0, v24 offset:256
	ds_write_b16_d16_hi v0, v24 offset:2320
	ds_write_b16 v0, v26 offset:4384
	ds_write_b16_d16_hi v0, v26 offset:6448
	s_waitcnt vmcnt(12)
	v_cvt_pk_bf16_f32 v28, v28, v29
	v_cvt_pk_bf16_f32 v30, v30, v31
	ds_write_b16 v0, v28 offset:384
	ds_write_b16_d16_hi v0, v28 offset:2448
	ds_write_b16 v0, v30 offset:4512
	ds_write_b16_d16_hi v0, v30 offset:6576
	s_waitcnt vmcnt(11)
	v_cvt_pk_bf16_f32 v32, v32, v33
	v_cvt_pk_bf16_f32 v34, v34, v35
	ds_write_b16 v0, v32 offset:512
	ds_write_b16_d16_hi v0, v32 offset:2576
	ds_write_b16 v0, v34 offset:4640
	ds_write_b16_d16_hi v0, v34 offset:6704
	s_waitcnt vmcnt(10)
	v_cvt_pk_bf16_f32 v36, v36, v37
	v_cvt_pk_bf16_f32 v38, v38, v39
	ds_write_b16 v0, v36 offset:640
	ds_write_b16_d16_hi v0, v36 offset:2704
	ds_write_b16 v0, v38 offset:4768
	ds_write_b16_d16_hi v0, v38 offset:6832
	s_waitcnt vmcnt(9)
	v_cvt_pk_bf16_f32 v40, v40, v41
	v_cvt_pk_bf16_f32 v42, v42, v43
	ds_write_b16 v0, v40 offset:768
	ds_write_b16_d16_hi v0, v40 offset:2832
	ds_write_b16 v0, v42 offset:4896
	ds_write_b16_d16_hi v0, v42 offset:6960
	s_waitcnt vmcnt(8)
	v_cvt_pk_bf16_f32 v44, v44, v45
	v_cvt_pk_bf16_f32 v46, v46, v47
	ds_write_b16 v0, v44 offset:896
	ds_write_b16_d16_hi v0, v44 offset:2960
	ds_write_b16 v0, v46 offset:5024
	ds_write_b16_d16_hi v0, v46 offset:7088
	s_waitcnt vmcnt(7)
	v_cvt_pk_bf16_f32 v48, v48, v49
	v_cvt_pk_bf16_f32 v50, v50, v51
	ds_write_b16 v0, v48 offset:1024
	ds_write_b16_d16_hi v0, v48 offset:3088
	ds_write_b16 v0, v50 offset:5152
	ds_write_b16_d16_hi v0, v50 offset:7216
	s_waitcnt vmcnt(6)
	v_cvt_pk_bf16_f32 v52, v52, v53
	v_cvt_pk_bf16_f32 v54, v54, v55
	ds_write_b16 v0, v52 offset:1152
	ds_write_b16_d16_hi v0, v52 offset:3216
	ds_write_b16 v0, v54 offset:5280
	ds_write_b16_d16_hi v0, v54 offset:7344
	s_waitcnt vmcnt(5)
	v_cvt_pk_bf16_f32 v56, v56, v57
	v_cvt_pk_bf16_f32 v58, v58, v59
	ds_write_b16 v0, v56 offset:1280
	ds_write_b16_d16_hi v0, v56 offset:3344
	ds_write_b16 v0, v58 offset:5408
	ds_write_b16_d16_hi v0, v58 offset:7472
	s_waitcnt vmcnt(4)
	v_cvt_pk_bf16_f32 v60, v60, v61
	v_cvt_pk_bf16_f32 v62, v62, v63
	ds_write_b16 v0, v60 offset:1408
	ds_write_b16_d16_hi v0, v60 offset:3472
	ds_write_b16 v0, v62 offset:5536
	ds_write_b16_d16_hi v0, v62 offset:7600
	s_waitcnt vmcnt(3)
	v_cvt_pk_bf16_f32 v64, v64, v65
	v_cvt_pk_bf16_f32 v66, v66, v67
	ds_write_b16 v0, v64 offset:1536
	ds_write_b16_d16_hi v0, v64 offset:3600
	ds_write_b16 v0, v66 offset:5664
	ds_write_b16_d16_hi v0, v66 offset:7728
	s_waitcnt vmcnt(2)
	v_cvt_pk_bf16_f32 v68, v68, v69
	v_cvt_pk_bf16_f32 v70, v70, v71
	ds_write_b16 v0, v68 offset:1664
	ds_write_b16_d16_hi v0, v68 offset:3728
	ds_write_b16 v0, v70 offset:5792
	ds_write_b16_d16_hi v0, v70 offset:7856
	s_waitcnt vmcnt(1)
	v_cvt_pk_bf16_f32 v72, v72, v73
	v_cvt_pk_bf16_f32 v74, v74, v75
	ds_write_b16 v0, v72 offset:1792
	ds_write_b16_d16_hi v0, v72 offset:3856
	ds_write_b16 v0, v74 offset:5920
	ds_write_b16_d16_hi v0, v74 offset:7984
	s_waitcnt vmcnt(0)
	v_cvt_pk_bf16_f32 v76, v76, v77
	v_cvt_pk_bf16_f32 v78, v78, v79
	ds_write_b16 v0, v76 offset:1920
	ds_write_b16_d16_hi v0, v76 offset:3984
	ds_write_b16 v0, v78 offset:6048
	ds_write_b16_d16_hi v0, v78 offset:8112
